# lever 1 (waitcnt placement): conversion points no longer drain the previous phase's stores at entry (LDS-only wait before the workgroup barrier)
# speedup vs baseline: 1.0085x; 1.0085x over previous
; #define LAS __attribute__((address_space(3)))
; __device__ __forceinline__ void phase_prologue(const Args& a, LAS unsigned char* lds) {
;     ...
;     unsigned* cq_head = (unsigned*)(a.ws + WS_CTL) + 8192 + 768;
;     volatile LAS int* qs = (volatile LAS int*)(lds + 128 * 129 * 4);
;     int pend = 0, it = 0;
;     if (tid == 0) { qs[0] = (int)xb_add(cq_head, 1u); pend = (int)xb_add(cq_head, 1u); }
;     __syncthreads();
;     for (int u = qs[0]; u < CTOT; u = qs[it & 1]) {
;         int r = u; const float* src; int ldn, nvalid, NT, mode = 0; bf16_t* dst;
;         if (r < CJ0) { src = a.in[I_EVIN]; ldn = 6144; nvalid = 6144; NT = 48; dst = (bf16_t*)(a.ws + WS_WIN0); }
;         else if ((r -= CJ0) < CJ1) { src = a.in[I_EVOUT]; ldn = 2048; nvalid = 2048; NT = 16; dst = (bf16_t*)(a.ws + WS_WOUT0); }
;         else if ((r -= CJ1) < CJ2) { src = a.in[I_ODIN]; ldn = 6176; nvalid = 6176; NT = 50; dst = (bf16_t*)(a.ws + WS_WIN1); }
;         else if ((r -= CJ2) < CJ3) { src = a.in[I_ODOUT]; ldn = 2048; nvalid = 2048; NT = 16; dst = (bf16_t*)(a.ws + WS_WOUT1); }
;         else { r -= CJ3; const int which = r / CJM; r -= which * CJM; const int mtx = r >> 8; r &= 255; ldn = 2048; nvalid = 2048; NT = 16;
;             if (which == 0) { src = a.in[I_WGATE] + (size_t)mtx * 2048 * 2048; dst = (bf16_t*)(a.ws + WS_WGU) + (size_t)mtx * 4096 * 2048; mode = 1; }
;             else if (which == 1) { src = a.in[I_WUP] + (size_t)mtx * 2048 * 2048; dst = (bf16_t*)(a.ws + WS_WGU) + (size_t)mtx * 4096 * 2048; mode = 2; }
;             else { src = a.in[I_WDOWN] + (size_t)mtx * 2048 * 2048; dst = (bf16_t*)(a.ws + WS_WDN) + (size_t)mtx * 2048 * 2048; } }
;         const int kt = r / NT, ntl = r % NT, k0 = kt * 128, n0 = ntl * 128;
;         const int drow0 = mode == 0 ? n0 : (ntl * 256 + (mode == 2 ? 128 : 0));
;         f32x4 v[8];
; #pragma unroll
;         for (int i = 0; i < 8; ++i) { const int id = tid + 512 * i, row = id >> 5, c4 = id & 31, n = n0 + c4 * 4;
;             v[i] = (f32x4){0.f, 0.f, 0.f, 0.f};
;             if (n < nvalid) v[i] = *(const f32x4*)(src + (size_t)(k0 + row) * ldn + n); }
; #pragma unroll
;         for (int i = 0; i < 8; ++i) { const int id = tid + 512 * i, row = id >> 5, c4 = id & 31;
;             LAS float* tp = tile + row * 129 + c4 * 4; tp[0] = v[i][0]; tp[1] = v[i][1]; tp[2] = v[i][2]; tp[3] = v[i][3]; }
;         lds_barrier();
; #pragma unroll
.LBB0_768:
.Lcvq0_entry:
	s_waitcnt lgkmcnt(0)
	s_barrier
	v_mov_b32_e32 v119, 1
	v_mov_b32_e32 v120, 0x9080
	v_mov_b32_e32 v122, 0
	v_mov_b32_e32 v125, 0x10200
	s_mov_b32 s67, 0
	v_lshrrev_b32_e32 v104, 5, v0
	v_and_b32_e32 v126, 31, v0
	v_lshlrev_b32_e32 v105, 13, v104
	v_lshl_add_u32 v105, v126, 4, v105
	v_add_u32_e32 v106, 0x20000, v105
	v_add_u32_e32 v107, 0x40000, v105
	v_add_u32_e32 v108, 0x60000, v105
	v_add_u32_e32 v109, 0x80000, v105
	v_add_u32_e32 v110, 0xa0000, v105
	v_add_u32_e32 v111, 0xc0000, v105
	v_add_u32_e32 v112, 0xe0000, v105
	v_mul_u32_u24_e32 v113, 0x204, v104
	v_lshl_add_u32 v113, v126, 4, v113
	v_lshrrev_b32_e32 v127, 4, v0
	v_and_b32_e32 v126, 15, v0
	v_mul_u32_u24_e32 v114, 0x1020, v126
	v_lshl_add_u32 v114, v127, 2, v114
	v_lshlrev_b32_e32 v115, 12, v127
	v_lshl_add_u32 v115, v126, 4, v115
	v_add_u32_e32 v116, 0x20000, v115
	v_add_u32_e32 v117, 0x40000, v115
	v_add_u32_e32 v118, 0x60000, v115
	v_readlane_b32 s82, v254, 27
	v_readlane_b32 s83, v254, 28
	s_sub_u32 s82, s82, 0x28
	s_subb_u32 s83, s83, 0
	s_load_dwordx2 s[80:81], s[82:83], 0x0
	s_waitcnt lgkmcnt(0)
	v_cmp_eq_u32_e32 vcc, 0, v0
	s_and_saveexec_b64 s[76:77], vcc
	s_cbranch_execz .Lcvq0_t0a
	global_atomic_add v123, v120, v119, s[94:95] sc0
	s_waitcnt vmcnt(0)
	ds_write_b32 v125, v123

; #define LAS __attribute__((address_space(3)))
; __device__ __forceinline__ unsigned xb_add(unsigned* p, unsigned v) { return __hip_atomic_fetch_add(p, v, __ATOMIC_RELAXED, __HIP_MEMORY_SCOPE_AGENT); }
; __device__ __forceinline__ void phase_prologue(const Args& a, LAS unsigned char* lds) {
;     ...
;     unsigned* cq_head = (unsigned*)(a.ws + WS_CTL) + 8192 + 768;
;     volatile LAS int* qs = (volatile LAS int*)(lds + 128 * 129 * 4);
;     int pend = 0, it = 0;
;     if (tid == 0) { qs[0] = (int)xb_add(cq_head, 1u); pend = (int)xb_add(cq_head, 1u); }
;     __syncthreads();
.Lcvq0_done:
.Lcvd_entry:
	s_waitcnt lgkmcnt(0)
	s_barrier
	v_mov_b32_e32 v119, 1
	v_mov_b32_e32 v120, 0x9000
	v_mov_b32_e32 v121, 0x9200
	v_mov_b32_e32 v122, 0
	v_mov_b32_e32 v125, 0x10200
	s_mov_b32 s67, 0
	v_cmp_eq_u32_e32 vcc, 0, v0
	s_and_saveexec_b64 s[76:77], vcc
	s_cbranch_execz .Lcvd_f0
	global_atomic_add v124, v121, v119, s[94:95] sc0
	s_waitcnt vmcnt(0)
	v_add_u32_e32 v124, 1, v124
	ds_write_b32 v125, v124 offset:4

; #define LAS __attribute__((address_space(3)))
; __device__ __forceinline__ unsigned xb_add(unsigned* p, unsigned v) { return __hip_atomic_fetch_add(p, v, __ATOMIC_RELAXED, __HIP_MEMORY_SCOPE_AGENT); }
; __device__ __forceinline__ void phase_prologue(const Args& a, LAS unsigned char* lds) {
;     ...
;     unsigned* cq_head = (unsigned*)(a.ws + WS_CTL) + 8192 + 768;
;     volatile LAS int* qs = (volatile LAS int*)(lds + 128 * 129 * 4);
;     int pend = 0, it = 0;
;     if (tid == 0) { qs[0] = (int)xb_add(cq_head, 1u); pend = (int)xb_add(cq_head, 1u); }
;     __syncthreads();
.Lcva_entry:
	s_waitcnt lgkmcnt(0)
	s_barrier
	v_mov_b32_e32 v119, 1
	v_mov_b32_e32 v120, 0x9000
	v_mov_b32_e32 v121, 0x9100
	v_mov_b32_e32 v122, 0
	v_mov_b32_e32 v125, 0x10200
	s_mov_b32 s25, 0
	v_cmp_eq_u32_e32 vcc, 0, v0
	s_and_saveexec_b64 s[34:35], vcc
	s_cbranch_execz .Lcva_f0
	global_atomic_add v124, v121, v122, s[94:95] sc0
	s_waitcnt vmcnt(0)
	ds_write_b32 v125, v124 offset:4

; #define LAS __attribute__((address_space(3)))
; __device__ __forceinline__ unsigned xb_add(unsigned* p, unsigned v) { return __hip_atomic_fetch_add(p, v, __ATOMIC_RELAXED, __HIP_MEMORY_SCOPE_AGENT); }
; __device__ __forceinline__ void phase_prologue(const Args& a, LAS unsigned char* lds) {
;     ...
;     unsigned* cq_head = (unsigned*)(a.ws + WS_CTL) + 8192 + 768;
;     volatile LAS int* qs = (volatile LAS int*)(lds + 128 * 129 * 4);
;     int pend = 0, it = 0;
;     if (tid == 0) { qs[0] = (int)xb_add(cq_head, 1u); pend = (int)xb_add(cq_head, 1u); }
;     __syncthreads();
.LBB0_1442:
.Lcvb_entry:
	s_waitcnt lgkmcnt(0)
	s_barrier
	v_mov_b32_e32 v119, 1
	v_mov_b32_e32 v120, 0x9000
	v_mov_b32_e32 v121, 0x9300
	v_mov_b32_e32 v122, 0
	v_mov_b32_e32 v125, 0x10200
	s_mov_b32 s25, 0
	v_cmp_eq_u32_e32 vcc, 0, v0
	s_and_saveexec_b64 s[34:35], vcc
	s_cbranch_execz .Lcvb_f0
	global_atomic_add v124, v121, v119, s[94:95] sc0
	s_waitcnt vmcnt(0)
	v_add_u32_e32 v124, 1, v124
	ds_write_b32 v125, v124 offset:4

; #define LAS __attribute__((address_space(3)))
; __device__ __forceinline__ void phase_prologue(const Args& a, LAS unsigned char* lds) {
;     ...
;     unsigned* cq_head = (unsigned*)(a.ws + WS_CTL) + 8192 + 768;
;     volatile LAS int* qs = (volatile LAS int*)(lds + 128 * 129 * 4);
;     int pend = 0, it = 0;
;     if (tid == 0) { qs[0] = (int)xb_add(cq_head, 1u); pend = (int)xb_add(cq_head, 1u); }
;     __syncthreads();
;     for (int u = qs[0]; u < CTOT; u = qs[it & 1]) {
;         int r = u; const float* src; int ldn, nvalid, NT, mode = 0; bf16_t* dst;
;         if (r < CJ0) { src = a.in[I_EVIN]; ldn = 6144; nvalid = 6144; NT = 48; dst = (bf16_t*)(a.ws + WS_WIN0); }
;         else if ((r -= CJ0) < CJ1) { src = a.in[I_EVOUT]; ldn = 2048; nvalid = 2048; NT = 16; dst = (bf16_t*)(a.ws + WS_WOUT0); }
;         else if ((r -= CJ1) < CJ2) { src = a.in[I_ODIN]; ldn = 6176; nvalid = 6176; NT = 50; dst = (bf16_t*)(a.ws + WS_WIN1); }
;         else if ((r -= CJ2) < CJ3) { src = a.in[I_ODOUT]; ldn = 2048; nvalid = 2048; NT = 16; dst = (bf16_t*)(a.ws + WS_WOUT1); }
;         else { r -= CJ3; const int which = r / CJM; r -= which * CJM; const int mtx = r >> 8; r &= 255; ldn = 2048; nvalid = 2048; NT = 16;
;             if (which == 0) { src = a.in[I_WGATE] + (size_t)mtx * 2048 * 2048; dst = (bf16_t*)(a.ws + WS_WGU) + (size_t)mtx * 4096 * 2048; mode = 1; }
;             else if (which == 1) { src = a.in[I_WUP] + (size_t)mtx * 2048 * 2048; dst = (bf16_t*)(a.ws + WS_WGU) + (size_t)mtx * 4096 * 2048; mode = 2; }
;             else { src = a.in[I_WDOWN] + (size_t)mtx * 2048 * 2048; dst = (bf16_t*)(a.ws + WS_WDN) + (size_t)mtx * 2048 * 2048; } }
;         const int kt = r / NT, ntl = r % NT, k0 = kt * 128, n0 = ntl * 128;
;         const int drow0 = mode == 0 ? n0 : (ntl * 256 + (mode == 2 ? 128 : 0));
;         f32x4 v[8];
; #pragma unroll
;         for (int i = 0; i < 8; ++i) { const int id = tid + 512 * i, row = id >> 5, c4 = id & 31, n = n0 + c4 * 4;
;             v[i] = (f32x4){0.f, 0.f, 0.f, 0.f};
;             if (n < nvalid) v[i] = *(const f32x4*)(src + (size_t)(k0 + row) * ldn + n); }
; #pragma unroll
;         for (int i = 0; i < 8; ++i) { const int id = tid + 512 * i, row = id >> 5, c4 = id & 31;
;             LAS float* tp = tile + row * 129 + c4 * 4; tp[0] = v[i][0]; tp[1] = v[i][1]; tp[2] = v[i][2]; tp[3] = v[i][3]; }
;         lds_barrier();
; #pragma unroll
.LBB0_1648:
.Lcvz_entry:
	s_waitcnt lgkmcnt(0)
	s_barrier
	v_mov_b32_e32 v119, 1
	v_mov_b32_e32 v120, 0x9000
	v_mov_b32_e32 v122, 0
	v_mov_b32_e32 v125, 0x10200
	s_mov_b32 s25, 0
	v_lshrrev_b32_e32 v104, 5, v0
	v_and_b32_e32 v126, 31, v0
	v_lshlrev_b32_e32 v105, 13, v104
	v_lshl_add_u32 v105, v126, 4, v105
	v_add_u32_e32 v106, 0x20000, v105
	v_add_u32_e32 v107, 0x40000, v105
	v_add_u32_e32 v108, 0x60000, v105
	v_add_u32_e32 v109, 0x80000, v105
	v_add_u32_e32 v110, 0xa0000, v105
	v_add_u32_e32 v111, 0xc0000, v105
	v_add_u32_e32 v112, 0xe0000, v105
	v_mul_u32_u24_e32 v113, 0x204, v104
	v_lshl_add_u32 v113, v126, 4, v113
	v_lshrrev_b32_e32 v127, 4, v0
	v_and_b32_e32 v126, 15, v0
	v_mul_u32_u24_e32 v114, 0x1020, v126
	v_lshl_add_u32 v114, v127, 2, v114
	v_lshlrev_b32_e32 v115, 12, v127
	v_lshl_add_u32 v115, v126, 4, v115
	v_add_u32_e32 v116, 0x20000, v115
	v_add_u32_e32 v117, 0x40000, v115
	v_add_u32_e32 v118, 0x60000, v115
	v_readlane_b32 s42, v254, 27
	v_readlane_b32 s43, v254, 28
	s_sub_u32 s42, s42, 0x28
	s_subb_u32 s43, s43, 0
	s_load_dwordx2 s[40:41], s[42:43], 0x0
	s_waitcnt lgkmcnt(0)
	v_cmp_eq_u32_e32 vcc, 0, v0
	s_and_saveexec_b64 s[34:35], vcc
	s_cbranch_execz .Lcvz_t0a
	global_atomic_add v123, v120, v119, s[94:95] sc0
	s_waitcnt vmcnt(0)
	ds_write_b32 v125, v123
